# sel block head: the third DMA piece (only waves 0-2 issue it) moved out of line so the other five waves fall through
# baseline (speedup 1.0000x reference)
; #define LAS __attribute__((address_space(3)))
; #define RD16(dst, base, off) asm volatile("ds_read_b128 %0, %1 offset:%2" : "=&v"(dst) : "v"(base), "i"(off) : "memory")
; __device__ __forceinline__ void ringS_dma(const RingSLane& R, const char* K8p, const char* VTp, LAS unsigned char* sb, int wave) {
;     __builtin_amdgcn_global_load_lds((const unsigned*)(K8p + R.so[0]), (LAS unsigned*)(sb + wave * 1024), 16, 0, 0);
;     __builtin_amdgcn_global_load_lds((const unsigned*)((wave == 0 ? K8p : VTp) + R.so[1]), (LAS unsigned*)(sb + (wave + 8) * 1024), 16, 0, 0);
;     if (wave <= 2) __builtin_amdgcn_global_load_lds((const unsigned*)(VTp + R.so[2]), (LAS unsigned*)(sb + (wave + 16) * 1024), 16, 0, 0);
; }
; __device__ __forceinline__ void qk8_tile_c(f32x4 (&s)[4], const GS8& g, const unsigned kb  , const float c0  ) {
;     i32x4a lo[4], hi[4];
;     RD16(lo[0], kb, 0); RD16(hi[0], kb, 16); RD16(lo[1], kb, 16 * K8ST); RD16(hi[1], kb, 16 * K8ST + 16);
.LBB0_1799:
	s_lshr_b32 s45, s67, s36
	s_and_b32 s97, s45, 0xff
	s_cbranch_scc0 .Lsel_notile
	ds_read_b128 v[84:87], v208 offset:0
	ds_read_b128 v[88:91], v208 offset:16
	ds_read_b128 v[92:95], v208 offset:0x900
	ds_read_b128 v[96:99], v208 offset:0x910
	ds_read_b128 v[118:121], v208 offset:0x1200
	ds_read_b128 v[122:125], v208 offset:0x1210
	s_bitcmp1_b32 s99, s37
	s_cbranch_scc0 .Lsel_tile2
	s_lshr_b32 vcc_lo, s60, s36
	s_and_b32 vcc_lo, vcc_lo, 0xff
	s_lshl_b32 vcc_lo, vcc_lo, 13
	s_add_u32 s12, s62, vcc_lo
	s_addc_u32 s13, s63, 0
	s_add_u32 s100, s64, vcc_lo
	s_addc_u32 s101, s65, 0
	s_mul_i32 vcc_hi, s37, 0x4c00
	s_add_i32 vcc_hi, s98, vcc_hi
	s_mov_b32 m0, vcc_hi
	s_cmp_lg_u64 s[16:17], 0
	global_load_lds_dwordx4 v102, s[12:13]
	s_cselect_b32 s13, s13, s101
	s_cselect_b32 s12, s12, s100
	s_add_i32 m0, vcc_hi, 0x2000
	s_cmp_lg_u64 s[10:11], 0
	global_load_lds_dwordx4 v106, s[12:13]
	s_cbranch_scc0 .Lsel_dma3

; #define LAS __attribute__((address_space(3)))
; __device__ __forceinline__ void ringS_dma(const RingSLane& R, const char* K8p, const char* VTp, LAS unsigned char* sb, int wave) {
;     ...
;     if (wave <= 2) __builtin_amdgcn_global_load_lds((const unsigned*)(VTp + R.so[2]), (LAS unsigned*)(sb + (wave + 16) * 1024), 16, 0, 0);
.Lsel_dma3:
	s_add_i32 m0, vcc_hi, 0x4000
	s_nop 0
	global_load_lds_dwordx4 v108, s[100:101]
	s_branch .Lsel_tile2
